# adaLN prologue GEMV: weights for the next 8-k step prefetched one iteration ahead (software pipelined), single vmcnt(0) at loop top
# speedup vs baseline: 1.0008x; 1.0008x over previous
.LBB0_76:
	s_mul_hi_i32 s4, s27, 0x2aaaaaab
	s_lshr_b32 s5, s4, 31
	s_ashr_i32 s10, s4, 4
	s_add_i32 s10, s10, s5
	s_mul_i32 s11, s10, 0x1800
	s_sub_i32 s4, s13, s11
	s_ashr_i32 s5, s4, 31
	s_mul_i32 s9, s10, 0x1800000
	s_lshl_b64 s[4:5], s[4:5], 2
	s_mul_hi_i32 s8, s10, 0x1800000
	s_add_u32 s4, s9, s4
	s_addc_u32 s5, s8, s5
	v_lshl_add_u64 v[58:59], v[56:57], 0, s[4:5]
	s_mov_b32 s8, -4
	v_mov_b32_e32 v87, v51
	v_mov_b32_e32 v60, 0
	v_mov_b32_e32 v61, v53
	v_mov_b32_e32 v62, 0
	v_mov_b32_e32 v63, v53
	v_mov_b32_e32 v64, 0
	v_mov_b32_e32 v65, v53
	v_mov_b32_e32 v66, 0
	v_mov_b32_e32 v67, v53
	v_mov_b32_e32 v68, 0
	v_mov_b32_e32 v69, v53
	v_mov_b32_e32 v70, 0
	v_mov_b32_e32 v71, v53
	v_mov_b32_e32 v72, 0
	v_mov_b32_e32 v73, v53
	v_mov_b32_e32 v74, 0
	v_mov_b32_e32 v75, v53
	v_mov_b32_e32 v88, 0
	global_load_dword v186, v[58:59], off
	v_add_co_u32_e64 v246, s[4:5], s14, v58
	s_nop 1
	v_addc_co_u32_e64 v247, s[4:5], -1, v59, s[4:5]
	global_load_dword v187, v[246:247], off
	v_add_co_u32_e64 v246, s[4:5], s15, v58
	s_nop 1
	v_addc_co_u32_e64 v247, s[4:5], -1, v59, s[4:5]
	global_load_dword v188, v[246:247], off
	v_add_co_u32_e64 v246, s[4:5], s16, v58
	s_nop 1
	v_addc_co_u32_e64 v247, s[4:5], -1, v59, s[4:5]
	global_load_dword v189, v[246:247], off
	v_add_co_u32_e64 v246, s[4:5], s17, v58
	s_nop 1
	v_addc_co_u32_e64 v247, s[4:5], -1, v59, s[4:5]
	global_load_dword v190, v[246:247], off
	v_add_co_u32_e64 v246, s[4:5], s12, v58
	s_nop 1
	v_addc_co_u32_e64 v247, s[4:5], 0, v59, s[4:5]
	global_load_dword v191, v[246:247], off
	v_add_co_u32_e64 v246, s[4:5], s18, v58
	s_nop 1
	v_addc_co_u32_e64 v247, s[4:5], 0, v59, s[4:5]
	global_load_dword v192, v[246:247], off
	v_add_co_u32_e64 v246, s[4:5], s19, v58
	s_nop 1
	v_addc_co_u32_e64 v247, s[4:5], 0, v59, s[4:5]
	global_load_dword v193, v[246:247], off
.LBB0_77:
	s_waitcnt vmcnt(0)
	v_mov_b32_e32 v84, v186
	v_mov_b32_e32 v176, v187
	v_mov_b32_e32 v178, v188
	v_mov_b32_e32 v180, v189
	v_mov_b32_e32 v182, v190
	v_mov_b32_e32 v170, v191
	v_mov_b32_e32 v172, v192
	v_mov_b32_e32 v174, v193
	s_cmp_lt_i32 s8, 0x74
	s_cselect_b32 s98, s2, 0
	s_cselect_b32 s99, s3, 0
	v_lshl_add_u64 v[194:195], v[58:59], 0, s[98:99]
	global_load_dword v186, v[194:195], off
	v_add_co_u32_e64 v246, s[4:5], s14, v194
	s_nop 1
	v_addc_co_u32_e64 v247, s[4:5], -1, v195, s[4:5]
	global_load_dword v187, v[246:247], off
	v_add_co_u32_e64 v246, s[4:5], s15, v194
	s_nop 1
	v_addc_co_u32_e64 v247, s[4:5], -1, v195, s[4:5]
	global_load_dword v188, v[246:247], off
	v_add_co_u32_e64 v246, s[4:5], s16, v194
	s_nop 1
	v_addc_co_u32_e64 v247, s[4:5], -1, v195, s[4:5]
	global_load_dword v189, v[246:247], off
	v_add_co_u32_e64 v246, s[4:5], s17, v194
	s_nop 1
	v_addc_co_u32_e64 v247, s[4:5], -1, v195, s[4:5]
	global_load_dword v190, v[246:247], off
	v_add_co_u32_e64 v246, s[4:5], s12, v194
	s_nop 1
	v_addc_co_u32_e64 v247, s[4:5], 0, v195, s[4:5]
	global_load_dword v191, v[246:247], off
	v_add_co_u32_e64 v246, s[4:5], s18, v194
	s_nop 1
	v_addc_co_u32_e64 v247, s[4:5], 0, v195, s[4:5]
	global_load_dword v192, v[246:247], off
	v_add_co_u32_e64 v246, s[4:5], s19, v194
	s_nop 1
	v_addc_co_u32_e64 v247, s[4:5], 0, v195, s[4:5]
	global_load_dword v193, v[246:247], off
	ds_read_b128 v[6:9], v87
	ds_read_b128 v[2:5], v87 offset:16
	v_add_u32_e32 v85, 0x10000, v87
	s_nop 0
	s_nop 0
	ds_read_b128 v[14:17], v87 offset:4096
	ds_read_b128 v[10:13], v87 offset:4112
	ds_read_b128 v[90:93], v87 offset:8192
	ds_read_b128 v[46:49], v87 offset:8208
	ds_read_b128 v[22:25], v87 offset:12288
	ds_read_b128 v[18:21], v87 offset:12304
	ds_read_b128 v[94:97], v87 offset:16384
	ds_read_b128 v[98:101], v87 offset:16400
	ds_read_b128 v[30:33], v87 offset:20480
	ds_read_b128 v[26:29], v87 offset:20496
	ds_read_b128 v[102:105], v87 offset:24576
	ds_read_b128 v[106:109], v87 offset:24592
	ds_read_b128 v[38:41], v87 offset:28672
	ds_read_b128 v[34:37], v87 offset:28688
	ds_read_b128 v[110:113], v87 offset:32768
	ds_read_b128 v[114:117], v87 offset:32784
	ds_read_b128 v[118:121], v87 offset:36864
	ds_read_b128 v[42:45], v87 offset:36880
	ds_read_b128 v[122:125], v87 offset:40960
	ds_read_b128 v[126:129], v87 offset:40976
	ds_read_b128 v[130:133], v87 offset:45056
	ds_read_b128 v[134:137], v87 offset:45072
	ds_read_b128 v[138:141], v87 offset:49152
	ds_read_b128 v[142:145], v87 offset:49168
	ds_read_b128 v[146:149], v87 offset:53248
	ds_read_b128 v[150:153], v87 offset:53264
	ds_read_b128 v[154:157], v87 offset:57344
	ds_read_b128 v[158:161], v87 offset:57360
	ds_read_b128 v[162:165], v87 offset:61440
	ds_read_b128 v[166:169], v87 offset:61456
	ds_read_b128 v[76:79], v85
	s_nop 0
	v_add_u32_e32 v89, 0x10010, v87
	s_nop 0
	s_nop 0
	s_nop 0
	ds_read_b128 v[80:83], v89
	s_waitcnt lgkmcnt(14)
	v_mov_b32_e32 v185, v14
	v_mov_b32_e32 v14, v7
	v_mov_b32_e32 v7, v16
	v_mov_b32_e32 v16, v9
	v_mov_b32_e32 v9, v22
	v_mov_b32_e32 v22, v91
	v_mov_b32_e32 v91, v24
	v_mov_b32_e32 v24, v93
	v_mov_b32_e32 v93, v30
	v_mov_b32_e32 v30, v95
	v_mov_b32_e32 v95, v32
	v_mov_b32_e32 v32, v97
	v_mov_b32_e32 v97, v38
	v_mov_b32_e32 v38, v103
	v_mov_b32_e32 v103, v40
	v_mov_b32_e32 v40, v105
	v_mov_b32_e32 v105, v118
	v_mov_b32_e32 v118, v111
	v_mov_b32_e32 v111, v120
	v_mov_b32_e32 v120, v113
	s_waitcnt lgkmcnt(11)
	v_mov_b32_e32 v113, v130
	v_mov_b32_e32 v130, v123
	v_mov_b32_e32 v123, v132
	v_mov_b32_e32 v132, v125
	s_waitcnt lgkmcnt(7)
	v_mov_b32_e32 v125, v146
	v_mov_b32_e32 v146, v139
	v_mov_b32_e32 v139, v148
	v_mov_b32_e32 v148, v141
	s_waitcnt lgkmcnt(3)
	v_mov_b32_e32 v141, v162
	v_mov_b32_e32 v162, v155
	v_mov_b32_e32 v184, v6
	v_mov_b32_e32 v6, v8
	v_mov_b32_e32 v8, v90
	v_mov_b32_e32 v90, v92
	v_mov_b32_e32 v92, v94
	v_mov_b32_e32 v94, v96
	v_mov_b32_e32 v96, v102
	v_mov_b32_e32 v102, v104
	v_mov_b32_e32 v104, v110
	v_mov_b32_e32 v110, v112
	v_mov_b32_e32 v112, v122
	v_mov_b32_e32 v122, v124
	v_mov_b32_e32 v124, v138
	v_mov_b32_e32 v138, v140
	v_mov_b32_e32 v140, v154
	v_mov_b32_e32 v154, v156
	v_mov_b32_e32 v155, v164
	v_mov_b32_e32 v164, v157
	v_mov_b32_e32 v156, v2
	v_mov_b32_e32 v157, v10
	v_mov_b32_e32 v10, v3
	v_mov_b32_e32 v2, v4
	v_mov_b32_e32 v3, v12
	v_mov_b32_e32 v12, v5
	v_mov_b32_e32 v4, v46
	v_mov_b32_e32 v5, v18
	v_mov_b32_e32 v18, v47
	v_mov_b32_e32 v46, v48
	v_mov_b32_e32 v47, v20
	v_mov_b32_e32 v20, v49
	v_mov_b32_e32 v48, v98
	v_mov_b32_e32 v49, v26
	v_mov_b32_e32 v26, v99
	v_mov_b32_e32 v98, v100
	v_mov_b32_e32 v99, v28
	v_mov_b32_e32 v28, v101
	v_mov_b32_e32 v100, v106
	v_mov_b32_e32 v101, v34
	v_mov_b32_e32 v34, v107
	v_mov_b32_e32 v106, v108
	v_mov_b32_e32 v107, v36
	v_mov_b32_e32 v36, v109
	v_mov_b32_e32 v108, v114
	v_mov_b32_e32 v109, v42
	v_mov_b32_e32 v42, v115
	v_mov_b32_e32 v114, v116
	v_mov_b32_e32 v115, v44
	v_mov_b32_e32 v44, v117
	v_mov_b32_e32 v116, v126
	v_mov_b32_e32 v117, v134
	v_mov_b32_e32 v134, v127
	v_mov_b32_e32 v126, v128
	v_mov_b32_e32 v127, v136
	v_mov_b32_e32 v136, v129
	v_mov_b32_e32 v128, v142
	v_mov_b32_e32 v129, v150
	v_mov_b32_e32 v150, v143
	v_mov_b32_e32 v142, v144
	v_mov_b32_e32 v143, v152
	v_mov_b32_e32 v152, v145
	v_mov_b32_e32 v144, v158
	s_waitcnt lgkmcnt(2)
	v_mov_b32_e32 v145, v166
	v_mov_b32_e32 v166, v159
	v_mov_b32_e32 v158, v160
	v_mov_b32_e32 v159, v168
	v_mov_b32_e32 v168, v161
	s_waitcnt lgkmcnt(1)
	v_mov_b32_e32 v160, v77
	v_mov_b32_e32 v161, v78
	v_mov_b32_e32 v77, v79
	s_waitcnt lgkmcnt(0)
	v_mov_b32_e32 v78, v81
	v_mov_b32_e32 v79, v82
	v_mov_b32_e32 v81, v83
	v_pk_mul_f32 v[14:15], v[178:179], v[14:15] op_sel_hi:[0,1]
	v_pk_mul_f32 v[16:17], v[182:183], v[16:17] op_sel_hi:[0,1]
	v_pk_mul_f32 v[22:23], v[178:179], v[22:23] op_sel_hi:[0,1]
	v_pk_mul_f32 v[24:25], v[182:183], v[24:25] op_sel_hi:[0,1]
	v_pk_mul_f32 v[30:31], v[178:179], v[30:31] op_sel_hi:[0,1]
	v_pk_mul_f32 v[32:33], v[182:183], v[32:33] op_sel_hi:[0,1]
	v_pk_mul_f32 v[38:39], v[178:179], v[38:39] op_sel_hi:[0,1]
	v_pk_mul_f32 v[40:41], v[182:183], v[40:41] op_sel_hi:[0,1]
	v_pk_mul_f32 v[82:83], v[178:179], v[118:119] op_sel_hi:[0,1]
	v_pk_mul_f32 v[118:119], v[182:183], v[120:121] op_sel_hi:[0,1]
	v_pk_mul_f32 v[120:121], v[178:179], v[130:131] op_sel_hi:[0,1]
	v_pk_mul_f32 v[130:131], v[182:183], v[132:133] op_sel_hi:[0,1]
	v_pk_mul_f32 v[132:133], v[178:179], v[146:147] op_sel_hi:[0,1]
	v_pk_mul_f32 v[146:147], v[182:183], v[148:149] op_sel_hi:[0,1]
	v_pk_mul_f32 v[148:149], v[178:179], v[162:163] op_sel_hi:[0,1]
	v_pk_mul_f32 v[162:163], v[182:183], v[164:165] op_sel_hi:[0,1]
	v_pk_mul_f32 v[10:11], v[170:171], v[10:11] op_sel_hi:[0,1]
	v_pk_mul_f32 v[12:13], v[174:175], v[12:13] op_sel_hi:[0,1]
	v_pk_mul_f32 v[18:19], v[170:171], v[18:19] op_sel_hi:[0,1]
	v_pk_mul_f32 v[20:21], v[174:175], v[20:21] op_sel_hi:[0,1]
	v_pk_mul_f32 v[26:27], v[170:171], v[26:27] op_sel_hi:[0,1]
	v_pk_mul_f32 v[28:29], v[174:175], v[28:29] op_sel_hi:[0,1]
	v_pk_mul_f32 v[34:35], v[170:171], v[34:35] op_sel_hi:[0,1]
	v_pk_mul_f32 v[36:37], v[174:175], v[36:37] op_sel_hi:[0,1]
	v_pk_mul_f32 v[42:43], v[170:171], v[42:43] op_sel_hi:[0,1]
	v_pk_mul_f32 v[44:45], v[174:175], v[44:45] op_sel_hi:[0,1]
	v_pk_mul_f32 v[134:135], v[170:171], v[134:135] op_sel_hi:[0,1]
	v_pk_mul_f32 v[150:151], v[170:171], v[150:151] op_sel_hi:[0,1]
	v_pk_mul_f32 v[164:165], v[170:171], v[166:167] op_sel_hi:[0,1]
	v_pk_fma_f32 v[14:15], v[176:177], v[184:185], v[14:15] op_sel_hi:[0,1,1]
	v_pk_fma_f32 v[6:7], v[180:181], v[6:7], v[16:17] op_sel_hi:[0,1,1]
	v_pk_fma_f32 v[8:9], v[176:177], v[8:9], v[22:23] op_sel_hi:[0,1,1]
	v_pk_fma_f32 v[16:17], v[180:181], v[90:91], v[24:25] op_sel_hi:[0,1,1]
	v_pk_fma_f32 v[22:23], v[176:177], v[92:93], v[30:31] op_sel_hi:[0,1,1]
	v_pk_fma_f32 v[24:25], v[180:181], v[94:95], v[32:33] op_sel_hi:[0,1,1]
	v_pk_fma_f32 v[30:31], v[176:177], v[96:97], v[38:39] op_sel_hi:[0,1,1]
	v_pk_fma_f32 v[32:33], v[180:181], v[102:103], v[40:41] op_sel_hi:[0,1,1]
	v_pk_fma_f32 v[38:39], v[176:177], v[104:105], v[82:83] op_sel_hi:[0,1,1]
	v_pk_fma_f32 v[40:41], v[180:181], v[110:111], v[118:119] op_sel_hi:[0,1,1]
	v_pk_fma_f32 v[82:83], v[176:177], v[112:113], v[120:121] op_sel_hi:[0,1,1]
	v_pk_fma_f32 v[92:93], v[176:177], v[124:125], v[132:133] op_sel_hi:[0,1,1]
	v_pk_fma_f32 v[96:97], v[176:177], v[140:141], v[148:149] op_sel_hi:[0,1,1]
	v_mov_b32_e32 v177, v182
	v_mov_b32_e32 v179, v180
	v_pk_fma_f32 v[10:11], v[84:85], v[156:157], v[10:11] op_sel_hi:[0,1,1]
	v_pk_fma_f32 v[2:3], v[172:173], v[2:3], v[12:13] op_sel_hi:[0,1,1]
	v_pk_fma_f32 v[4:5], v[84:85], v[4:5], v[18:19] op_sel_hi:[0,1,1]
	v_pk_fma_f32 v[12:13], v[172:173], v[46:47], v[20:21] op_sel_hi:[0,1,1]
	v_pk_fma_f32 v[18:19], v[84:85], v[48:49], v[26:27] op_sel_hi:[0,1,1]
	v_pk_fma_f32 v[20:21], v[172:173], v[98:99], v[28:29] op_sel_hi:[0,1,1]
	v_pk_fma_f32 v[26:27], v[84:85], v[100:101], v[34:35] op_sel_hi:[0,1,1]
	v_pk_fma_f32 v[28:29], v[172:173], v[106:107], v[36:37] op_sel_hi:[0,1,1]
	v_pk_fma_f32 v[34:35], v[84:85], v[108:109], v[42:43] op_sel_hi:[0,1,1]
	v_pk_fma_f32 v[36:37], v[172:173], v[114:115], v[44:45] op_sel_hi:[0,1,1]
	v_pk_fma_f32 v[42:43], v[84:85], v[116:117], v[134:135] op_sel_hi:[0,1,1]
	v_pk_fma_f32 v[46:47], v[84:85], v[128:129], v[150:151] op_sel_hi:[0,1,1]
	v_pk_fma_f32 v[98:99], v[84:85], v[144:145], v[164:165] op_sel_hi:[0,1,1]
	v_mov_b32_e32 v85, v174
	v_pk_add_f32 v[6:7], v[14:15], v[6:7]
	v_pk_add_f32 v[14:15], v[22:23], v[24:25]
	v_pk_add_f32 v[22:23], v[38:39], v[40:41]
	v_pk_mul_f32 v[38:39], v[176:177], v[76:77]
	v_pk_mul_f32 v[136:137], v[174:175], v[136:137] op_sel_hi:[0,1]
	v_pk_mul_f32 v[152:153], v[174:175], v[152:153] op_sel_hi:[0,1]
	v_pk_mul_f32 v[166:167], v[174:175], v[168:169] op_sel_hi:[0,1]
	v_mov_b32_e32 v171, v172
	v_pk_fma_f32 v[90:91], v[180:181], v[122:123], v[130:131] op_sel_hi:[0,1,1]
	v_pk_fma_f32 v[94:95], v[180:181], v[138:139], v[146:147] op_sel_hi:[0,1,1]
	v_pk_fma_f32 v[102:103], v[180:181], v[154:155], v[162:163] op_sel_hi:[0,1,1]
	v_pk_add_f32 v[2:3], v[10:11], v[2:3]
	v_pk_add_f32 v[10:11], v[18:19], v[20:21]
	v_pk_add_f32 v[18:19], v[34:35], v[36:37]
	v_pk_mul_f32 v[34:35], v[84:85], v[80:81]
	v_pk_fma_f32 v[36:37], v[178:179], v[160:161], v[38:39]
	v_pk_fma_f32 v[44:45], v[172:173], v[126:127], v[136:137] op_sel_hi:[0,1,1]
	v_pk_fma_f32 v[48:49], v[172:173], v[142:143], v[152:153] op_sel_hi:[0,1,1]
	v_pk_fma_f32 v[100:101], v[172:173], v[158:159], v[166:167] op_sel_hi:[0,1,1]
	v_pk_add_f32 v[8:9], v[8:9], v[16:17]
	v_pk_add_f32 v[16:17], v[30:31], v[32:33]
	v_pk_add_f32 v[24:25], v[82:83], v[90:91]
	v_pk_add_f32 v[30:31], v[92:93], v[94:95]
	v_pk_add_f32 v[32:33], v[96:97], v[102:103]
	v_pk_add_f32 v[6:7], v[60:61], v[6:7]
	v_pk_fma_f32 v[34:35], v[170:171], v[78:79], v[34:35]
	v_add_f32_e32 v36, v36, v37
	s_add_i32 s8, s8, 8
	v_pk_add_f32 v[4:5], v[4:5], v[12:13]
	v_pk_add_f32 v[12:13], v[26:27], v[28:29]
	v_pk_add_f32 v[20:21], v[42:43], v[44:45]
	v_pk_add_f32 v[26:27], v[46:47], v[48:49]
	v_pk_add_f32 v[28:29], v[98:99], v[100:101]
	v_pk_add_f32 v[8:9], v[62:63], v[8:9]
	v_pk_add_f32 v[14:15], v[64:65], v[14:15]
	v_pk_add_f32 v[16:17], v[66:67], v[16:17]
	v_pk_add_f32 v[22:23], v[68:69], v[22:23]
	v_pk_add_f32 v[24:25], v[70:71], v[24:25]
	v_pk_add_f32 v[30:31], v[72:73], v[30:31]
	v_pk_add_f32 v[32:33], v[74:75], v[32:33]
	v_pk_add_f32 v[60:61], v[6:7], v[2:3]
	v_add_f32_e32 v2, v34, v35
	v_add_f32_e32 v3, v88, v36
	v_add_u32_e32 v87, 32, v87
	v_lshl_add_u64 v[58:59], v[58:59], 0, s[2:3]
	s_cmpk_gt_u32 s8, 0x7b
	v_pk_add_f32 v[62:63], v[8:9], v[4:5]
	v_pk_add_f32 v[64:65], v[14:15], v[10:11]
	v_pk_add_f32 v[66:67], v[16:17], v[12:13]
	v_pk_add_f32 v[68:69], v[22:23], v[18:19]
	v_pk_add_f32 v[70:71], v[24:25], v[20:21]
	v_pk_add_f32 v[72:73], v[30:31], v[26:27]
	v_pk_add_f32 v[74:75], v[32:33], v[28:29]
	v_add_f32_e32 v88, v3, v2
	s_cbranch_scc0 .LBB0_77
	ds_write2st64_b32 v52, v60, v61 offset1:1
	ds_write2st64_b32 v52, v62, v63 offset0:2 offset1:3
	ds_write2st64_b32 v52, v64, v65 offset0:4 offset1:5
	ds_write2st64_b32 v52, v66, v67 offset0:6 offset1:7
	ds_write2st64_b32 v52, v68, v69 offset0:8 offset1:9
	ds_write2st64_b32 v52, v70, v71 offset0:10 offset1:11
	ds_write2st64_b32 v52, v72, v73 offset0:12 offset1:13
	ds_write2st64_b32 v52, v74, v75 offset0:14 offset1:15
	ds_write_b32 v52, v88 offset:4096
	s_waitcnt lgkmcnt(0)
	s_barrier
	s_and_saveexec_b64 s[8:9], vcc
	s_cbranch_execz .LBB0_75
	s_mul_i32 s4, s10, 0xffffffa0
	s_add_i32 s4, s4, s27
	s_lshl_b32 s4, s4, 6
	s_add_i32 s11, s4, s11
	v_or_b32_e32 v2, s11, v1
	s_ashr_i32 s5, s4, 31
	v_ashrrev_i32_e32 v3, 31, v2
	s_mul_i32 s21, s10, 17
	v_lshl_add_u64 v[2:3], v[2:3], 2, s[6:7]
	v_lshl_add_u64 v[4:5], s[4:5], 2, v[54:55]
	s_mov_b64 s[10:11], 0
	v_mov_b32_e32 v6, v50
